# P0: odd waves stream x->bf16 first, even waves weight transposes first (overlap); plus select + inversion
# speedup vs baseline: 1.0151x; 1.0065x over previous
.LBB0_7:
	s_or_b64 exec, exec, s[0:1]
	s_add_u32 s6, s50, 0x200000
	s_addc_u32 s7, s51, 0
	s_add_u32 s0, s50, 0xa00000
	s_addc_u32 s1, s51, 0
	s_add_u32 s8, s50, 0xc00000
	s_addc_u32 s9, s51, 0
	v_writelane_b32 v252, s0, 4
	s_add_u32 s3, s50, 0x9800000
	s_addc_u32 s68, s51, 0
	v_writelane_b32 v252, s1, 5
	s_add_u32 s69, s50, 0xb800000
	v_readlane_b32 s0, v252, 2
	s_addc_u32 s70, s51, 0
	s_lshr_b32 s1, s10, 6
	s_lshl_b32 s0, s0, 3
	s_add_i32 s96, s0, s1
	s_lshl_b32 s92, s84, 3
	v_writelane_b32 v252, s1, 6
	s_cmp_lt_i32 s88, 1
	v_writelane_b32 v252, s0, 7
	s_cselect_b64 s[0:1], -1, 0
	s_cmp_gt_i32 s89, 0
	s_cselect_b64 s[4:5], -1, 0
	s_and_b64 s[0:1], s[0:1], s[4:5]
	s_andn2_b64 vcc, exec, s[0:1]
	v_and_b32_e32 v198, 63, v0
	s_cbranch_vccnz .LBB0_135
	v_readlane_b32 s99, v252, 6
	s_mov_b32 s98, 0
	s_bitcmp1_b32 s99, 0
	s_cbranch_scc0 .Lp0_weights
	s_mov_b32 s98, 1
	s_mov_b32 s99, s36
	s_branch .LBB0_59
.Lp0_weights:
	s_cmpk_gt_i32 s96, 0xaff
	s_cbranch_scc1 .LBB0_56
	v_readlane_b32 s0, v252, 6
	s_lshl_b32 s0, s0, 14
	s_add_i32 s0, s0, 0
	v_and_b32_e32 v1, 31, v0
	v_lshrrev_b32_e32 v6, 5, v198
	v_lshlrev_b32_e32 v2, 3, v0
	v_lshl_add_u32 v4, v1, 2, s0
	v_mul_u32_u24_e32 v5, 0x84, v6
	v_lshrrev_b32_e32 v7, 3, v198
	v_and_b32_e32 v2, 56, v2
	v_mul_u32_u24_e32 v8, 0x84, v2
	v_lshlrev_b32_e32 v9, 2, v7
	v_add_u32_e32 v12, v4, v5
	s_mov_b32 s1, 0
	v_mov_b32_e32 v3, 0
	v_add3_u32 v8, s0, v8, v9
	v_or_b32_e32 v9, 8, v7
	v_or_b32_e32 v10, 16, v7
	v_or_b32_e32 v11, 24, v7
	s_movk_i32 s18, 0x7ff
	s_movk_i32 s19, 0xfc3
	s_movk_i32 s20, 0xfc7
	s_movk_i32 s21, 0xfd0
	v_lshlrev_b32_e32 v4, 1, v2
	v_add_u32_e32 v13, 0x400, v12
	v_add_u32_e32 v14, 0x800, v12
	v_add_u32_e32 v15, 0xc00, v12
	v_add_u32_e32 v16, 0x1000, v12
	v_add_u32_e32 v17, 0x1400, v12
	v_add_u32_e32 v18, 0x1800, v12
	v_add_u32_e32 v19, 0x1c00, v12
	s_mov_b32 s22, s96
	s_branch .LBB0_13

.LBB0_59:
	s_cmp_eq_u32 s98, 2
	s_cbranch_scc1 .LBB0_78
	s_cmpk_gt_i32 s96, 0x47ff
	s_cbranch_scc1 .LBB0_78
	s_add_i32 s18, s96, 0xffffc000
	s_mul_i32 s19, s84, 40
	s_lshl_b32 s20, s84, 4
	s_mul_i32 s21, s84, 24
	s_lshl_b32 s22, s84, 5
	v_lshlrev_b32_e32 v1, 4, v198
	s_branch .LBB0_62

.LBB0_78:
	s_cmp_eq_u32 s98, 1
	s_cbranch_scc0 .Lp0_done
	s_mov_b32 s98, 2
	s_mov_b32 s36, s99
	s_branch .Lp0_weights
